# lean_r1
# baseline (speedup 1.0000x reference)
_Z10gae_kernelPKfPKiS2_S0_S0_S0_PfS3_:
	s_cmp_ge_u32 s2, 0x2000
	s_cbranch_scc1 .Lgae_exit
	s_load_dwordx8 s[4:11], s[0:1], 0x0
	s_load_dwordx8 s[12:19], s[0:1], 0x20
	v_and_b32_e32 v4, 63, v0
	v_lshrrev_b32_e32 v5, 6, v0
	v_sub_u32_e32 v1, 63, v4
	v_lshlrev_b32_e32 v1, 4, v1
	v_lshl_or_b32 v2, v5, 11, v1
	s_lshl_b32 s20, s2, 13
	v_add_u32_e32 v2, s20, v2
	v_mov_b32_e32 v3, v2
	v_lshlrev_b32_e32 v7, 2, v5
	v_mov_b32_e32 v8, 0
	s_movk_i32 s50, 0xc0
	s_movk_i32 s51, 0x80
	v_cmp_gt_u32_e64 s[24:25], s50, v0
	v_cmp_gt_u32_e64 s[26:27], s51, v0
	v_cmp_gt_u32_e64 s[28:29], 64, v0
	s_movk_i32 s21, 1
	s_waitcnt lgkmcnt(0)
	global_load_dwordx4 v[50:53], v2, s[14:15] nt
	global_load_dwordx4 v[54:57], v2, s[14:15] offset:1024 nt
	global_load_dwordx4 v[18:21], v2, s[6:7] nt
	global_load_dwordx4 v[22:25], v2, s[6:7] offset:1024 nt
	global_load_dwordx4 v[26:29], v2, s[8:9] nt
	global_load_dwordx4 v[30:33], v2, s[8:9] offset:1024 nt
	global_load_dwordx4 v[42:45], v2, s[12:13] nt
	global_load_dwordx4 v[46:49], v2, s[12:13] offset:1024 nt
	global_load_dwordx4 v[10:13], v2, s[4:5] nt
	global_load_dwordx4 v[14:17], v2, s[4:5] offset:1024 nt
	global_load_dwordx4 v[34:37], v2, s[10:11] nt
	global_load_dwordx4 v[38:41], v2, s[10:11] offset:1024 nt
	s_waitcnt vmcnt(0)
.Lgae_loop:
	s_waitcnt vmcnt(4)
	v_cmp_eq_u32_e64 s[30:31], 0, v18
	v_cmp_eq_u32_e64 s[32:33], 0, v19
	v_cmp_eq_u32_e64 s[34:35], 0, v20
	v_cmp_eq_u32_e64 s[36:37], 0, v21
	v_cmp_eq_u32_e64 s[38:39], 0, v26
	v_cmp_eq_u32_e64 s[40:41], 0, v27
	v_cmp_eq_u32_e64 s[42:43], 0, v28
	v_cmp_eq_u32_e64 s[44:45], 0, v29
	v_mul_f32_e32 v50, 0x3f7d70a4, v50
	v_mul_f32_e32 v51, 0x3f7d70a4, v51
	v_mul_f32_e32 v52, 0x3f7d70a4, v52
	v_mul_f32_e32 v53, 0x3f7d70a4, v53
	v_mul_f32_e32 v42, v42, v50
	v_mul_f32_e32 v43, v43, v51
	v_mul_f32_e32 v44, v44, v52
	v_mul_f32_e32 v45, v45, v53
	v_cndmask_b32_e64 v18, 0, 1.0, s[30:31]
	v_cndmask_b32_e64 v19, 0, 1.0, s[32:33]
	v_cndmask_b32_e64 v20, 0, 1.0, s[34:35]
	v_cndmask_b32_e64 v21, 0, 1.0, s[36:37]
	v_cndmask_b32_e64 v26, 0, 1.0, s[38:39]
	v_cndmask_b32_e64 v27, 0, 1.0, s[40:41]
	v_cndmask_b32_e64 v28, 0, 1.0, s[42:43]
	v_cndmask_b32_e64 v29, 0, 1.0, s[44:45]
	v_fma_f32 v58, v42, v18, v10
	v_fma_f32 v59, v43, v19, v11
	v_fma_f32 v60, v44, v20, v12
	v_fma_f32 v61, v45, v21, v13
	v_mul_f32_e32 v50, 0x3f733333, v50
	v_mul_f32_e32 v51, 0x3f733333, v51
	v_mul_f32_e32 v52, 0x3f733333, v52
	v_mul_f32_e32 v53, 0x3f733333, v53
	v_sub_f32_e32 v58, v58, v34
	v_sub_f32_e32 v59, v59, v35
	v_sub_f32_e32 v60, v60, v36
	v_sub_f32_e32 v61, v61, v37
	v_mul_f32_e32 v66, v50, v26
	v_mul_f32_e32 v67, v51, v27
	v_mul_f32_e32 v68, v52, v28
	v_mul_f32_e32 v69, v53, v29
	v_mov_b32_e32 v74, v34
	v_mov_b32_e32 v75, v35
	v_mov_b32_e32 v76, v36
	v_mov_b32_e32 v77, v37
	v_cmp_eq_u32_e64 s[30:31], 0, v22
	v_cmp_eq_u32_e64 s[32:33], 0, v23
	v_cmp_eq_u32_e64 s[34:35], 0, v24
	v_cmp_eq_u32_e64 s[36:37], 0, v25
	v_cmp_eq_u32_e64 s[38:39], 0, v30
	v_cmp_eq_u32_e64 s[40:41], 0, v31
	v_cmp_eq_u32_e64 s[42:43], 0, v32
	v_cmp_eq_u32_e64 s[44:45], 0, v33
	v_mul_f32_e32 v54, 0x3f7d70a4, v54
	v_mul_f32_e32 v55, 0x3f7d70a4, v55
	v_mul_f32_e32 v56, 0x3f7d70a4, v56
	v_mul_f32_e32 v57, 0x3f7d70a4, v57
	v_mul_f32_e32 v46, v46, v54
	v_mul_f32_e32 v47, v47, v55
	v_mul_f32_e32 v48, v48, v56
	v_mul_f32_e32 v49, v49, v57
	v_cndmask_b32_e64 v22, 0, 1.0, s[30:31]
	v_cndmask_b32_e64 v23, 0, 1.0, s[32:33]
	v_cndmask_b32_e64 v24, 0, 1.0, s[34:35]
	v_cndmask_b32_e64 v25, 0, 1.0, s[36:37]
	v_cndmask_b32_e64 v30, 0, 1.0, s[38:39]
	v_cndmask_b32_e64 v31, 0, 1.0, s[40:41]
	v_cndmask_b32_e64 v32, 0, 1.0, s[42:43]
	v_cndmask_b32_e64 v33, 0, 1.0, s[44:45]
	v_fma_f32 v62, v46, v22, v14
	v_fma_f32 v63, v47, v23, v15
	v_fma_f32 v64, v48, v24, v16
	v_fma_f32 v65, v49, v25, v17
	v_mul_f32_e32 v54, 0x3f733333, v54
	v_mul_f32_e32 v55, 0x3f733333, v55
	v_mul_f32_e32 v56, 0x3f733333, v56
	v_mul_f32_e32 v57, 0x3f733333, v57
	v_sub_f32_e32 v62, v62, v38
	v_sub_f32_e32 v63, v63, v39
	v_sub_f32_e32 v64, v64, v40
	v_sub_f32_e32 v65, v65, v41
	v_mul_f32_e32 v70, v54, v30
	v_mul_f32_e32 v71, v55, v31
	v_mul_f32_e32 v72, v56, v32
	v_mul_f32_e32 v73, v57, v33
	v_mov_b32_e32 v78, v38
	v_mov_b32_e32 v79, v39
	v_mov_b32_e32 v80, v40
	v_mov_b32_e32 v81, v41
	s_cmp_eq_u32 s21, 1
	s_cbranch_scc1 .Lgae_nopf
	v_add_u32_e32 v2, 0x4000000, v2
	global_load_dwordx4 v[50:53], v2, s[14:15] nt
	global_load_dwordx4 v[54:57], v2, s[14:15] offset:1024 nt
	global_load_dwordx4 v[18:21], v2, s[6:7] nt
	global_load_dwordx4 v[22:25], v2, s[6:7] offset:1024 nt
	global_load_dwordx4 v[26:29], v2, s[8:9] nt
	global_load_dwordx4 v[30:33], v2, s[8:9] offset:1024 nt
	global_load_dwordx4 v[42:45], v2, s[12:13] nt
	global_load_dwordx4 v[46:49], v2, s[12:13] offset:1024 nt
	global_load_dwordx4 v[10:13], v2, s[4:5] nt
	global_load_dwordx4 v[14:17], v2, s[4:5] offset:1024 nt
	global_load_dwordx4 v[34:37], v2, s[10:11] nt
	global_load_dwordx4 v[38:41], v2, s[10:11] offset:1024 nt
.Lgae_nopf:
	v_fma_f32 v83, v68, v61, v60
	v_mul_f32_e32 v82, v68, v69
	v_fma_f32 v83, v67, v83, v59
	v_mul_f32_e32 v82, v67, v82
	v_fma_f32 v83, v66, v83, v58
	v_mul_f32_e32 v82, v66, v82
	v_fma_f32 v85, v72, v65, v64
	v_mul_f32_e32 v84, v72, v73
	v_fma_f32 v85, v71, v85, v63
	v_mul_f32_e32 v84, v71, v84
	v_fma_f32 v85, v70, v85, v62
	v_mul_f32_e32 v84, v70, v84
	s_nop 1
	v_fmac_f32_dpp v83, v83, v82 row_shr:1 row_mask:0xf bank_mask:0xf
	v_mul_f32_dpp v82, v82, v82 row_shr:1 row_mask:0xf bank_mask:0xf
	v_fmac_f32_dpp v85, v85, v84 row_shr:1 row_mask:0xf bank_mask:0xf
	v_mul_f32_dpp v84, v84, v84 row_shr:1 row_mask:0xf bank_mask:0xf
	v_fmac_f32_dpp v83, v83, v82 row_shr:2 row_mask:0xf bank_mask:0xf
	v_mul_f32_dpp v82, v82, v82 row_shr:2 row_mask:0xf bank_mask:0xf
	v_fmac_f32_dpp v85, v85, v84 row_shr:2 row_mask:0xf bank_mask:0xf
	v_mul_f32_dpp v84, v84, v84 row_shr:2 row_mask:0xf bank_mask:0xf
	v_fmac_f32_dpp v83, v83, v82 row_shr:4 row_mask:0xf bank_mask:0xf
	v_mul_f32_dpp v82, v82, v82 row_shr:4 row_mask:0xf bank_mask:0xf
	v_fmac_f32_dpp v85, v85, v84 row_shr:4 row_mask:0xf bank_mask:0xf
	v_mul_f32_dpp v84, v84, v84 row_shr:4 row_mask:0xf bank_mask:0xf
	v_fmac_f32_dpp v83, v83, v82 row_shr:8 row_mask:0xf bank_mask:0xf
	v_mul_f32_dpp v82, v82, v82 row_shr:8 row_mask:0xf bank_mask:0xf
	v_fmac_f32_dpp v85, v85, v84 row_shr:8 row_mask:0xf bank_mask:0xf
	v_mul_f32_dpp v84, v84, v84 row_shr:8 row_mask:0xf bank_mask:0xf
	v_fmac_f32_dpp v83, v83, v82 row_bcast:15 row_mask:0xa bank_mask:0xf
	v_mul_f32_dpp v82, v82, v82 row_bcast:15 row_mask:0xa bank_mask:0xf
	v_fmac_f32_dpp v85, v85, v84 row_bcast:15 row_mask:0xa bank_mask:0xf
	v_mul_f32_dpp v84, v84, v84 row_bcast:15 row_mask:0xa bank_mask:0xf
	v_fmac_f32_dpp v83, v83, v82 row_bcast:31 row_mask:0xc bank_mask:0xf
	v_mul_f32_dpp v82, v82, v82 row_bcast:31 row_mask:0xc bank_mask:0xf
	v_fmac_f32_dpp v85, v85, v84 row_bcast:31 row_mask:0xc bank_mask:0xf
	v_mul_f32_dpp v84, v84, v84 row_bcast:31 row_mask:0xc bank_mask:0xf
	s_nop 1
	v_readlane_b32 s46, v83, 63
	v_readlane_b32 s47, v82, 63
	v_readlane_b32 s48, v85, 63
	v_readlane_b32 s49, v84, 63
	s_nop 3
	v_mov_b32_e32 v86, s49
	v_mov_b32_e32 v87, s48
	v_mov_b32_e32 v88, s46
	v_mul_f32_e32 v86, s47, v86
	v_fmac_f32_e32 v88, s47, v87
	ds_write2_b32 v7, v86, v88 offset1:4
	s_waitcnt lgkmcnt(0)
	s_barrier
	ds_read_b128 v[90:93], v8
	ds_read_b128 v[94:97], v8 offset:16
	s_waitcnt lgkmcnt(0)
	v_cndmask_b32_e64 v89, 0, v97, s[24:25]
	v_fma_f32 v98, v92, v89, v96
	v_cndmask_b32_e64 v89, v89, v98, s[26:27]
	v_fma_f32 v98, v91, v89, v95
	v_cndmask_b32_e64 v89, v89, v98, s[28:29]
	v_mov_b32_e32 v99, s48
	v_fmac_f32_e32 v99, s49, v89
	v_fmac_f32_e32 v83, v82, v99
	v_fmac_f32_e32 v85, v84, v89
	s_nop 1
	v_mov_b32_dpp v99, v83 wave_shr:1 row_mask:0xf bank_mask:0xf
	v_mov_b32_dpp v89, v85 wave_shr:1 row_mask:0xf bank_mask:0xf
	v_fmac_f32_e32 v61, v69, v99
	v_fmac_f32_e32 v65, v73, v89
	v_fmac_f32_e32 v60, v68, v61
	v_fmac_f32_e32 v64, v72, v65
	v_fmac_f32_e32 v59, v67, v60
	v_fmac_f32_e32 v63, v71, v64
	v_fmac_f32_e32 v58, v66, v59
	v_fmac_f32_e32 v62, v70, v63
	v_pk_add_f32 v[74:75], v[58:59], v[74:75]
	v_pk_add_f32 v[76:77], v[60:61], v[76:77]
	v_pk_add_f32 v[78:79], v[62:63], v[78:79]
	v_pk_add_f32 v[80:81], v[64:65], v[80:81]
	global_store_dwordx4 v3, v[58:61], s[16:17] nt
	global_store_dwordx4 v3, v[62:65], s[16:17] offset:1024 nt
	global_store_dwordx4 v3, v[74:77], s[18:19] nt
	global_store_dwordx4 v3, v[78:81], s[18:19] offset:1024 nt
	v_mov_b32_e32 v3, v2
	v_xor_b32_e32 v7, 32, v7
	v_xor_b32_e32 v8, 32, v8
	s_sub_u32 s21, s21, 1
	s_cmp_lg_u32 s21, 0
	s_cbranch_scc1 .Lgae_loop
.Lgae_exit:
	s_endpgm

	.amdhsa_kernel _Z10gae_kernelPKfPKiS2_S0_S0_S0_PfS3_
		.amdhsa_group_segment_fixed_size 81664
		.amdhsa_private_segment_fixed_size 0
		.amdhsa_kernarg_size 64
		.amdhsa_user_sgpr_count 2
		.amdhsa_user_sgpr_dispatch_ptr 0
		.amdhsa_user_sgpr_queue_ptr 0
		.amdhsa_user_sgpr_kernarg_segment_ptr 1
		.amdhsa_user_sgpr_dispatch_id 0
		.amdhsa_user_sgpr_kernarg_preload_length 0
		.amdhsa_user_sgpr_kernarg_preload_offset 0
		.amdhsa_user_sgpr_private_segment_size 0
		.amdhsa_uses_dynamic_stack 0
		.amdhsa_enable_private_segment 0
		.amdhsa_system_sgpr_workgroup_id_x 1
		.amdhsa_system_sgpr_workgroup_id_y 0
		.amdhsa_system_sgpr_workgroup_id_z 0
		.amdhsa_system_sgpr_workgroup_info 0
		.amdhsa_system_vgpr_workitem_id 0
		.amdhsa_next_free_vgpr 104
		.amdhsa_next_free_sgpr 96
		.amdhsa_accum_offset 100
		.amdhsa_reserve_vcc 1
		.amdhsa_float_round_mode_32 0
		.amdhsa_float_round_mode_16_64 0
		.amdhsa_float_denorm_mode_32 3
		.amdhsa_float_denorm_mode_16_64 3
		.amdhsa_dx10_clamp 1
		.amdhsa_ieee_mode 1
		.amdhsa_fp16_overflow 0
		.amdhsa_tg_split 0
		.amdhsa_exception_fp_ieee_invalid_op 0
		.amdhsa_exception_fp_denorm_src 0
		.amdhsa_exception_fp_ieee_div_zero 0
		.amdhsa_exception_fp_ieee_overflow 0
		.amdhsa_exception_fp_ieee_underflow 0
		.amdhsa_exception_fp_ieee_inexact 0
		.amdhsa_exception_int_div_zero 0
	.end_amdhsa_kernel

.Lfunc_end0:
	.size	_Z10gae_kernelPKfPKiS2_S0_S0_S0_PfS3_, .Lfunc_end0-_Z10gae_kernelPKfPKiS2_S0_S0_S0_PfS3_
	.set _Z10gae_kernelPKfPKiS2_S0_S0_S0_PfS3_.num_vgpr, 100
	.set _Z10gae_kernelPKfPKiS2_S0_S0_S0_PfS3_.num_agpr, 0
	.set _Z10gae_kernelPKfPKiS2_S0_S0_S0_PfS3_.numbered_sgpr, 16
	.set _Z10gae_kernelPKfPKiS2_S0_S0_S0_PfS3_.num_named_barrier, 0
	.set _Z10gae_kernelPKfPKiS2_S0_S0_S0_PfS3_.private_seg_size, 0
	.set _Z10gae_kernelPKfPKiS2_S0_S0_S0_PfS3_.uses_vcc, 1
	.set _Z10gae_kernelPKfPKiS2_S0_S0_S0_PfS3_.uses_flat_scratch, 0
	.set _Z10gae_kernelPKfPKiS2_S0_S0_S0_PfS3_.has_dyn_sized_stack, 0
	.set _Z10gae_kernelPKfPKiS2_S0_S0_S0_PfS3_.has_recursion, 0
	.set _Z10gae_kernelPKfPKiS2_S0_S0_S0_PfS3_.has_indirect_call, 0

amdhsa.kernels:
  - .agpr_count:     0
    .args:
      - .actual_access:  read_only
        .address_space:  global
        .offset:         0
        .size:           8
        .value_kind:     global_buffer
      - .actual_access:  read_only
        .address_space:  global
        .offset:         8
        .size:           8
        .value_kind:     global_buffer
      - .actual_access:  read_only
        .address_space:  global
        .offset:         16
        .size:           8
        .value_kind:     global_buffer
      - .actual_access:  read_only
        .address_space:  global
        .offset:         24
        .size:           8
        .value_kind:     global_buffer
      - .actual_access:  read_only
        .address_space:  global
        .offset:         32
        .size:           8
        .value_kind:     global_buffer
      - .actual_access:  read_only
        .address_space:  global
        .offset:         40
        .size:           8
        .value_kind:     global_buffer
      - .actual_access:  write_only
        .address_space:  global
        .offset:         48
        .size:           8
        .value_kind:     global_buffer
      - .actual_access:  write_only
        .address_space:  global
        .offset:         56
        .size:           8
        .value_kind:     global_buffer
    .group_segment_fixed_size: 81664
    .kernarg_segment_align: 8
    .kernarg_segment_size: 64
    .language:       OpenCL C
    .language_version:
      - 2
      - 0
    .max_flat_workgroup_size: 256
    .name:           _Z10gae_kernelPKfPKiS2_S0_S0_S0_PfS3_
    .private_segment_fixed_size: 0
    .sgpr_count:     22
    .sgpr_spill_count: 0
    .symbol:         _Z10gae_kernelPKfPKiS2_S0_S0_S0_PfS3_.kd
    .uniform_work_group_size: 1
    .uses_dynamic_stack: false
    .vgpr_count:     100
    .vgpr_spill_count: 0
    .wavefront_size: 64
